# add P11 SwiGLU bias via LDS-DMA prefetch (opt6) and unrolled P0 silu table loads (opt7)
# speedup vs baseline: 1.0046x; 1.0046x over previous
; __device__ __forceinline__ float sigmoidf_(float x) { return __builtin_amdgcn_rcpf(1.0f + __expf(-x)); }
; __device__ __forceinline__ void p0_prologue(Frame& F, const Args& args) {
;     ...
;     for (int i = F.tid; i < NB * D; i += 512) { const int b = i / D, k = i % D; const float cv = args.in[1][i]; sc[k * 8 + b] = cv * sigmoidf_(cv); }
.LBB0_9:
	s_mov_b64 s[100:101], 0x1000
	global_load_dword v10, v[2:3], off
	global_load_dword v11, v[2:3], off offset:2048
	v_lshl_add_u64 v[2:3], v[2:3], 0, s[100:101]
	global_load_dword v12, v[2:3], off
	global_load_dword v13, v[2:3], off offset:2048
	v_lshl_add_u64 v[2:3], v[2:3], 0, s[100:101]
	global_load_dword v14, v[2:3], off
	global_load_dword v15, v[2:3], off offset:2048
	v_lshl_add_u64 v[2:3], v[2:3], 0, s[100:101]
	global_load_dword v16, v[2:3], off
	global_load_dword v17, v[2:3], off offset:2048
	v_lshl_add_u64 v[2:3], v[2:3], 0, s[100:101]
	global_load_dword v18, v[2:3], off
	global_load_dword v19, v[2:3], off offset:2048
	v_lshl_add_u64 v[2:3], v[2:3], 0, s[100:101]
	global_load_dword v20, v[2:3], off
	global_load_dword v21, v[2:3], off offset:2048
	v_lshl_add_u64 v[2:3], v[2:3], 0, s[100:101]
	global_load_dword v22, v[2:3], off
	global_load_dword v23, v[2:3], off offset:2048
	v_lshl_add_u64 v[2:3], v[2:3], 0, s[100:101]
	global_load_dword v24, v[2:3], off
	global_load_dword v25, v[2:3], off offset:2048
	v_lshl_add_u64 v[2:3], v[2:3], 0, s[100:101]
	global_load_dword v26, v[2:3], off
	global_load_dword v27, v[2:3], off offset:2048
	v_lshl_add_u64 v[2:3], v[2:3], 0, s[100:101]
	global_load_dword v28, v[2:3], off
	global_load_dword v29, v[2:3], off offset:2048
	v_lshl_add_u64 v[2:3], v[2:3], 0, s[100:101]
	global_load_dword v30, v[2:3], off
	global_load_dword v31, v[2:3], off offset:2048
	v_lshl_add_u64 v[2:3], v[2:3], 0, s[100:101]
	global_load_dword v32, v[2:3], off
	global_load_dword v33, v[2:3], off offset:2048
	v_lshl_add_u64 v[2:3], v[2:3], 0, s[100:101]
	global_load_dword v34, v[2:3], off
	global_load_dword v35, v[2:3], off offset:2048
	v_lshl_add_u64 v[2:3], v[2:3], 0, s[100:101]
	global_load_dword v36, v[2:3], off
	global_load_dword v37, v[2:3], off offset:2048
	v_lshl_add_u64 v[2:3], v[2:3], 0, s[100:101]
	global_load_dword v38, v[2:3], off
	global_load_dword v39, v[2:3], off offset:2048
	v_lshl_add_u64 v[2:3], v[2:3], 0, s[100:101]
	global_load_dword v40, v[2:3], off
	global_load_dword v41, v[2:3], off offset:2048
	v_lshl_add_u64 v[2:3], v[2:3], 0, s[100:101]
	v_add_u32_e32 v7, s2, v1
	s_waitcnt vmcnt(30)
	v_mul_f32_e32 v8, 0xbfb8aa3b, v10
	v_mul_f32_e32 v9, 0xbfb8aa3b, v11
	v_exp_f32_e32 v8, v8
	v_exp_f32_e32 v9, v9
	s_nop 0
	v_add_f32_e32 v8, 1.0, v8
	v_add_f32_e32 v9, 1.0, v9
	v_rcp_f32_e32 v8, v8
	v_rcp_f32_e32 v9, v9
	s_nop 0
	v_mul_f32_e32 v10, v10, v8
	v_mul_f32_e32 v11, v11, v9
	ds_write_b32 v7, v10 offset:0
	ds_write_b32 v7, v11 offset:16384
	s_waitcnt vmcnt(28)
	v_mul_f32_e32 v8, 0xbfb8aa3b, v12
	v_mul_f32_e32 v9, 0xbfb8aa3b, v13
	v_exp_f32_e32 v8, v8
	v_exp_f32_e32 v9, v9
	s_nop 0
	v_add_f32_e32 v8, 1.0, v8
	v_add_f32_e32 v9, 1.0, v9
	v_rcp_f32_e32 v8, v8
	v_rcp_f32_e32 v9, v9
	s_nop 0
	v_mul_f32_e32 v12, v12, v8
	v_mul_f32_e32 v13, v13, v9
	ds_write_b32 v7, v12 offset:32768
	ds_write_b32 v7, v13 offset:49152
	s_waitcnt vmcnt(26)
	v_mul_f32_e32 v8, 0xbfb8aa3b, v14
	v_mul_f32_e32 v9, 0xbfb8aa3b, v15
	v_exp_f32_e32 v8, v8
	v_exp_f32_e32 v9, v9
	s_nop 0
	v_add_f32_e32 v8, 1.0, v8
	v_add_f32_e32 v9, 1.0, v9
	v_rcp_f32_e32 v8, v8
	v_rcp_f32_e32 v9, v9
	s_nop 0
	v_mul_f32_e32 v14, v14, v8
	v_mul_f32_e32 v15, v15, v9
	ds_write_b32 v7, v14 offset:4
	ds_write_b32 v7, v15 offset:16388
	s_waitcnt vmcnt(24)
	v_mul_f32_e32 v8, 0xbfb8aa3b, v16
	v_mul_f32_e32 v9, 0xbfb8aa3b, v17
	v_exp_f32_e32 v8, v8
	v_exp_f32_e32 v9, v9
	s_nop 0
	v_add_f32_e32 v8, 1.0, v8
	v_add_f32_e32 v9, 1.0, v9
	v_rcp_f32_e32 v8, v8
	v_rcp_f32_e32 v9, v9
	s_nop 0
	v_mul_f32_e32 v16, v16, v8
	v_mul_f32_e32 v17, v17, v9
	ds_write_b32 v7, v16 offset:32772
	ds_write_b32 v7, v17 offset:49156
	s_waitcnt vmcnt(22)
	v_mul_f32_e32 v8, 0xbfb8aa3b, v18
	v_mul_f32_e32 v9, 0xbfb8aa3b, v19
	v_exp_f32_e32 v8, v8
	v_exp_f32_e32 v9, v9
	s_nop 0
	v_add_f32_e32 v8, 1.0, v8
	v_add_f32_e32 v9, 1.0, v9
	v_rcp_f32_e32 v8, v8
	v_rcp_f32_e32 v9, v9
	s_nop 0
	v_mul_f32_e32 v18, v18, v8
	v_mul_f32_e32 v19, v19, v9
	ds_write_b32 v7, v18 offset:8
	ds_write_b32 v7, v19 offset:16392
	s_waitcnt vmcnt(20)
	v_mul_f32_e32 v8, 0xbfb8aa3b, v20
	v_mul_f32_e32 v9, 0xbfb8aa3b, v21
	v_exp_f32_e32 v8, v8
	v_exp_f32_e32 v9, v9
	s_nop 0
	v_add_f32_e32 v8, 1.0, v8
	v_add_f32_e32 v9, 1.0, v9
	v_rcp_f32_e32 v8, v8
	v_rcp_f32_e32 v9, v9
	s_nop 0
	v_mul_f32_e32 v20, v20, v8
	v_mul_f32_e32 v21, v21, v9
	ds_write_b32 v7, v20 offset:32776
	ds_write_b32 v7, v21 offset:49160
	s_waitcnt vmcnt(18)
; __device__ __forceinline__ float sigmoidf_(float x) { return __builtin_amdgcn_rcpf(1.0f + __expf(-x)); }
; __device__ __forceinline__ void p0_prologue(Frame& F, const Args& args) {
;     ...
;     for (int i = F.tid; i < NB * D; i += 512) { const int b = i / D, k = i % D; const float cv = args.in[1][i]; sc[k * 8 + b] = cv * sigmoidf_(cv); }
;     __syncthreads();
;     {
;         float* modp = (float*)(ws + WS_MODP);
;         for (int it = gw; it < 16 * 48; it += NGW) {
;             const int kc = it / 48, jc = it % 48, j0 = jc * 256 + 4 * F.lane;
	v_mul_f32_e32 v8, 0xbfb8aa3b, v22
	v_mul_f32_e32 v9, 0xbfb8aa3b, v23
	v_exp_f32_e32 v8, v8
	v_exp_f32_e32 v9, v9
	s_nop 0
	v_add_f32_e32 v8, 1.0, v8
	v_add_f32_e32 v9, 1.0, v9
	v_rcp_f32_e32 v8, v8
	v_rcp_f32_e32 v9, v9
	s_nop 0
	v_mul_f32_e32 v22, v22, v8
	v_mul_f32_e32 v23, v23, v9
	ds_write_b32 v7, v22 offset:12
	ds_write_b32 v7, v23 offset:16396
	s_waitcnt vmcnt(16)
	v_mul_f32_e32 v8, 0xbfb8aa3b, v24
	v_mul_f32_e32 v9, 0xbfb8aa3b, v25
	v_exp_f32_e32 v8, v8
	v_exp_f32_e32 v9, v9
	s_nop 0
	v_add_f32_e32 v8, 1.0, v8
	v_add_f32_e32 v9, 1.0, v9
	v_rcp_f32_e32 v8, v8
	v_rcp_f32_e32 v9, v9
	s_nop 0
	v_mul_f32_e32 v24, v24, v8
	v_mul_f32_e32 v25, v25, v9
	ds_write_b32 v7, v24 offset:32780
	ds_write_b32 v7, v25 offset:49164
	s_waitcnt vmcnt(14)
	v_mul_f32_e32 v8, 0xbfb8aa3b, v26
	v_mul_f32_e32 v9, 0xbfb8aa3b, v27
	v_exp_f32_e32 v8, v8
	v_exp_f32_e32 v9, v9
	s_nop 0
	v_add_f32_e32 v8, 1.0, v8
	v_add_f32_e32 v9, 1.0, v9
	v_rcp_f32_e32 v8, v8
	v_rcp_f32_e32 v9, v9
	s_nop 0
	v_mul_f32_e32 v26, v26, v8
	v_mul_f32_e32 v27, v27, v9
	ds_write_b32 v7, v26 offset:16
	ds_write_b32 v7, v27 offset:16400
	s_waitcnt vmcnt(12)
	v_mul_f32_e32 v8, 0xbfb8aa3b, v28
	v_mul_f32_e32 v9, 0xbfb8aa3b, v29
	v_exp_f32_e32 v8, v8
	v_exp_f32_e32 v9, v9
	s_nop 0
	v_add_f32_e32 v8, 1.0, v8
	v_add_f32_e32 v9, 1.0, v9
	v_rcp_f32_e32 v8, v8
	v_rcp_f32_e32 v9, v9
	s_nop 0
	v_mul_f32_e32 v28, v28, v8
	v_mul_f32_e32 v29, v29, v9
	ds_write_b32 v7, v28 offset:32784
	ds_write_b32 v7, v29 offset:49168
	s_waitcnt vmcnt(10)
	v_mul_f32_e32 v8, 0xbfb8aa3b, v30
	v_mul_f32_e32 v9, 0xbfb8aa3b, v31
	v_exp_f32_e32 v8, v8
	v_exp_f32_e32 v9, v9
	s_nop 0
	v_add_f32_e32 v8, 1.0, v8
	v_add_f32_e32 v9, 1.0, v9
	v_rcp_f32_e32 v8, v8
	v_rcp_f32_e32 v9, v9
	s_nop 0
	v_mul_f32_e32 v30, v30, v8
	v_mul_f32_e32 v31, v31, v9
	ds_write_b32 v7, v30 offset:20
	ds_write_b32 v7, v31 offset:16404
	s_waitcnt vmcnt(8)
	v_mul_f32_e32 v8, 0xbfb8aa3b, v32
	v_mul_f32_e32 v9, 0xbfb8aa3b, v33
	v_exp_f32_e32 v8, v8
	v_exp_f32_e32 v9, v9
	s_nop 0
	v_add_f32_e32 v8, 1.0, v8
	v_add_f32_e32 v9, 1.0, v9
	v_rcp_f32_e32 v8, v8
	v_rcp_f32_e32 v9, v9
	s_nop 0
	v_mul_f32_e32 v32, v32, v8
	v_mul_f32_e32 v33, v33, v9
	ds_write_b32 v7, v32 offset:32788
	ds_write_b32 v7, v33 offset:49172
	s_waitcnt vmcnt(6)
	v_mul_f32_e32 v8, 0xbfb8aa3b, v34
	v_mul_f32_e32 v9, 0xbfb8aa3b, v35
	v_exp_f32_e32 v8, v8
	v_exp_f32_e32 v9, v9
	s_nop 0
	v_add_f32_e32 v8, 1.0, v8
	v_add_f32_e32 v9, 1.0, v9
	v_rcp_f32_e32 v8, v8
	v_rcp_f32_e32 v9, v9
	s_nop 0
	v_mul_f32_e32 v34, v34, v8
	v_mul_f32_e32 v35, v35, v9
	ds_write_b32 v7, v34 offset:24
	ds_write_b32 v7, v35 offset:16408
	s_waitcnt vmcnt(4)
	v_mul_f32_e32 v8, 0xbfb8aa3b, v36
	v_mul_f32_e32 v9, 0xbfb8aa3b, v37
	v_exp_f32_e32 v8, v8
	v_exp_f32_e32 v9, v9
	s_nop 0
	v_add_f32_e32 v8, 1.0, v8
	v_add_f32_e32 v9, 1.0, v9
	v_rcp_f32_e32 v8, v8
	v_rcp_f32_e32 v9, v9
	s_nop 0
	v_mul_f32_e32 v36, v36, v8
	v_mul_f32_e32 v37, v37, v9
	ds_write_b32 v7, v36 offset:32792
	ds_write_b32 v7, v37 offset:49176
	s_waitcnt vmcnt(2)
	v_mul_f32_e32 v8, 0xbfb8aa3b, v38
	v_mul_f32_e32 v9, 0xbfb8aa3b, v39
	v_exp_f32_e32 v8, v8
	v_exp_f32_e32 v9, v9
	s_nop 0
	v_add_f32_e32 v8, 1.0, v8
	v_add_f32_e32 v9, 1.0, v9
	v_rcp_f32_e32 v8, v8
	v_rcp_f32_e32 v9, v9
	s_nop 0
	v_mul_f32_e32 v38, v38, v8
	v_mul_f32_e32 v39, v39, v9
	ds_write_b32 v7, v38 offset:28
	ds_write_b32 v7, v39 offset:16412
	s_waitcnt vmcnt(0)
	v_mul_f32_e32 v8, 0xbfb8aa3b, v40
	v_mul_f32_e32 v9, 0xbfb8aa3b, v41
	v_exp_f32_e32 v8, v8
	v_exp_f32_e32 v9, v9
	s_nop 0
	v_add_f32_e32 v8, 1.0, v8
	v_add_f32_e32 v9, 1.0, v9
	v_rcp_f32_e32 v8, v8
	v_rcp_f32_e32 v9, v9
	s_nop 0
	v_mul_f32_e32 v40, v40, v8
	v_mul_f32_e32 v41, v41, v9
	ds_write_b32 v7, v40 offset:32796
	ds_write_b32 v7, v41 offset:49180
	s_or_b64 exec, exec, s[0:1]
	s_lshl_b32 s21, s94, 3
	s_add_i32 s21, s21, s96
	s_lshl_b32 s2, s93, 3
	s_cmpk_lt_i32 s21, 0x300
	s_cselect_b64 s[0:1], -1, 0
	s_max_i32 s18, s2, 0
	s_add_i32 s3, s2, 0xfffffd00
	s_cmpk_gt_i32 s93, 0x60
	s_cselect_b32 s3, s3, 0
	s_cmpk_gt_i32 s21, 0x2ff
	v_lshlrev_b32_e32 v60, 2, v224
	s_waitcnt lgkmcnt(0)
	s_barrier
	s_cbranch_scc1 .LBB0_15
	s_add_u32 s16, s50, 0x200000
	v_readlane_b32 s52, v253, 12
	s_addc_u32 s17, s51, 0
	v_readlane_b32 s56, v253, 16
	v_readlane_b32 s57, v253, 17
	s_add_u32 s19, s56, 0x30000
	s_addc_u32 s20, s57, 0
	v_mov_b32_e32 v61, 0xc000
	s_mov_b32 s22, s21
	v_readlane_b32 s53, v253, 13
	v_readlane_b32 s54, v253, 14
	v_readlane_b32 s55, v253, 15
	v_readlane_b32 s58, v253, 18
	v_readlane_b32 s59, v253, 19
	v_readlane_b32 s60, v253, 20
	v_readlane_b32 s61, v253, 21
	v_readlane_b32 s62, v253, 22
	v_readlane_b32 s63, v253, 23
	v_readlane_b32 s64, v253, 24
	v_readlane_b32 s65, v253, 25
	v_readlane_b32 s66, v253, 26
	v_readlane_b32 s67, v253, 27

;     __device__ __forceinline__ void operator()(const f32x4 (&acc)[2][2][4][2], const Unit& u, int wr, int wc, int fr, int fq) const {
;     ...
;         const float* bb = bias + (size_t)u.e * 2 * de + cl;
;         f32x4 bg[2], bl[2];
; #pragma unroll
;         for (int n = 0; n < 2; ++n) { bg[n] = *(const f32x4*)(bb + 4 * n); bl[n] = *(const f32x4*)(bb + de + 4 * n); }
; template <class Epi, class Sched, bool ALIGN_EPI = false, bool SP2 = false, bool GATHER = false, bool F8 = false>
; __device__ __forceinline__ void gemm_phase(PG8_LAS unsigned char* lds, const Gemm g, const Sched& S, const Epi& E) {
;     ...
; #pragma unroll
;         for (int a = 0; a < 2; ++a)
; #pragma unroll
;             for (int b = 0; b < 2; ++b)
; #pragma unroll
;                 for (int m = 0; m < 4; ++m)
; #pragma unroll
;                     for (int n = 0; n < 2; ++n) acc[a][b][m][n] = (f32x4){0.f, 0.f, 0.f, 0.f}; }
;         cur = nxt; cA = nA; cB = nB; ++ui;
.LBB0_1385:
	s_ashr_i32 s55, s54, 31
	s_lshl_b64 s[56:57], s[54:55], 23
	s_add_u32 s53, s2, s56
	s_addc_u32 s55, s3, s57
	s_ashr_i32 s37, s36, 31
	s_lshl_b64 s[56:57], s[36:37], 19
	s_add_u32 s56, s53, s56
	s_addc_u32 s57, s55, s57
	s_and_b64 s[4:5], s[4:5], exec
	s_cselect_b32 s37, s57, s63
	s_cselect_b32 s53, s56, s62
	v_mov_b32_e32 v175, v163
	v_mov_b32_e32 v177, v163
	s_add_u32 s55, s62, 0x100
	v_mov_b32_e32 v34, 0
	s_addc_u32 s76, s63, 0
	v_lshl_add_u64 v[178:179], s[16:17], 0, v[176:177]
	v_lshl_add_u64 v[180:181], s[16:17], 0, v[174:175]
	s_mov_b32 s77, -2
	s_mov_b64 s[64:65], 0
	v_mov_b32_e32 v35, v34
	v_mov_b32_e32 v36, v34
	v_mov_b32_e32 v37, v34
	v_mov_b32_e32 v42, v34
	v_mov_b32_e32 v43, v34
	v_mov_b32_e32 v44, v34
	v_mov_b32_e32 v45, v34
	v_mov_b32_e32 v50, v34
	v_mov_b32_e32 v51, v34
	v_mov_b32_e32 v52, v34
	v_mov_b32_e32 v53, v34
	v_mov_b32_e32 v58, v34
	v_mov_b32_e32 v59, v34
	v_mov_b32_e32 v60, v34
	v_mov_b32_e32 v61, v34
	v_mov_b32_e32 v66, v34
	v_mov_b32_e32 v67, v34
	v_mov_b32_e32 v68, v34
	v_mov_b32_e32 v69, v34
	v_mov_b32_e32 v74, v34
	v_mov_b32_e32 v75, v34
	v_mov_b32_e32 v76, v34
	v_mov_b32_e32 v77, v34
	v_mov_b32_e32 v82, v34
	v_mov_b32_e32 v83, v34
	v_mov_b32_e32 v84, v34
	v_mov_b32_e32 v85, v34
	v_mov_b32_e32 v90, v34
	v_mov_b32_e32 v91, v34
	v_mov_b32_e32 v92, v34
	v_mov_b32_e32 v93, v34
	v_mov_b32_e32 v38, v34
	v_mov_b32_e32 v39, v34
	v_mov_b32_e32 v40, v34
	v_mov_b32_e32 v41, v34
	v_mov_b32_e32 v46, v34
	v_mov_b32_e32 v47, v34
	v_mov_b32_e32 v48, v34
	v_mov_b32_e32 v49, v34
	v_mov_b32_e32 v54, v34
	v_mov_b32_e32 v55, v34
	v_mov_b32_e32 v56, v34
	v_mov_b32_e32 v57, v34
	v_mov_b32_e32 v62, v34
	v_mov_b32_e32 v63, v34
	v_mov_b32_e32 v64, v34
	v_mov_b32_e32 v65, v34
	v_mov_b32_e32 v70, v34
	v_mov_b32_e32 v71, v34
	v_mov_b32_e32 v72, v34
	v_mov_b32_e32 v73, v34
	v_mov_b32_e32 v78, v34
	v_mov_b32_e32 v79, v34
	v_mov_b32_e32 v80, v34
	v_mov_b32_e32 v81, v34
	v_mov_b32_e32 v86, v34
	v_mov_b32_e32 v87, v34
	v_mov_b32_e32 v88, v34
	v_mov_b32_e32 v89, v34
	v_mov_b32_e32 v94, v34
	v_mov_b32_e32 v95, v34
	v_mov_b32_e32 v96, v34
	v_mov_b32_e32 v97, v34
	v_mov_b32_e32 v98, v34
	v_mov_b32_e32 v99, v34
	v_mov_b32_e32 v100, v34
	v_mov_b32_e32 v101, v34
	v_mov_b32_e32 v106, v34
	v_mov_b32_e32 v107, v34
	v_mov_b32_e32 v108, v34
	v_mov_b32_e32 v109, v34
	v_mov_b32_e32 v114, v34
	v_mov_b32_e32 v115, v34
	v_mov_b32_e32 v116, v34
	v_mov_b32_e32 v117, v34
	v_mov_b32_e32 v122, v34
	v_mov_b32_e32 v123, v34
	v_mov_b32_e32 v124, v34
	v_mov_b32_e32 v125, v34
	v_mov_b32_e32 v130, v34
	v_mov_b32_e32 v131, v34
	v_mov_b32_e32 v132, v34
	v_mov_b32_e32 v133, v34
	v_mov_b32_e32 v138, v34
	v_mov_b32_e32 v139, v34
	v_mov_b32_e32 v140, v34
	v_mov_b32_e32 v141, v34
	v_mov_b32_e32 v146, v34
	v_mov_b32_e32 v147, v34
	v_mov_b32_e32 v148, v34
	v_mov_b32_e32 v149, v34
	v_mov_b32_e32 v150, v34
	v_mov_b32_e32 v151, v34
	v_mov_b32_e32 v152, v34
	v_mov_b32_e32 v153, v34
	v_mov_b32_e32 v102, v34
	v_mov_b32_e32 v103, v34
	v_mov_b32_e32 v104, v34
	v_mov_b32_e32 v105, v34
	v_mov_b32_e32 v110, v34
	v_mov_b32_e32 v111, v34
	v_mov_b32_e32 v112, v34
	v_mov_b32_e32 v113, v34
	v_mov_b32_e32 v118, v34
	v_mov_b32_e32 v119, v34
	v_mov_b32_e32 v120, v34
	v_mov_b32_e32 v121, v34
	v_mov_b32_e32 v126, v34
	v_mov_b32_e32 v127, v34
	v_mov_b32_e32 v128, v34
	v_mov_b32_e32 v129, v34
	v_mov_b32_e32 v134, v34
	v_mov_b32_e32 v135, v34
	v_mov_b32_e32 v136, v34
	v_mov_b32_e32 v137, v34
	v_mov_b32_e32 v142, v34
	v_mov_b32_e32 v143, v34
	v_mov_b32_e32 v144, v34
	v_mov_b32_e32 v145, v34
	v_mov_b32_e32 v154, v34
	v_mov_b32_e32 v155, v34
	v_mov_b32_e32 v156, v34
	v_mov_b32_e32 v157, v34
	v_mov_b32_e32 v158, v34
	v_mov_b32_e32 v159, v34
	v_mov_b32_e32 v160, v34
	v_mov_b32_e32 v161, v34
	v_and_b32_e32 v246, 31, v224
	v_and_b32_e32 v247, 0x60, v196
	v_add_u32_e32 v246, v246, v247
	v_lshl_add_u32 v246, s60, 7, v246
	v_lshlrev_b32_e32 v246, 2, v246
	v_and_b32_e32 v247, 32, v224
	v_lshl_add_u32 v246, v247, 8, v246
	v_lshl_add_u32 v246, v170, 14, v246
	v_mov_b32_e32 v247, 0
	v_lshl_add_u64 v[244:245], s[40:41], 0, v[246:247]
	s_lshl_b32 s100, s96, 8
	s_add_i32 m0, s100, 0x20800
	s_nop 0
	global_load_lds_dword v[244:245], off

;     __device__ __forceinline__ void operator()(const f32x4 (&acc)[2][2][4][2], const Unit& u, int wr, int wc, int fr, int fq) const {
;         const int row0 = u.pm * BM + wr * 64 + fr, cl = u.pn * HALF + wc * 32 + 8 * fq;
;         const float* bb = bias + (size_t)u.e * 2 * de + cl;
;         f32x4 bg[2], bl[2];
; #pragma unroll
;         for (int n = 0; n < 2; ++n) { bg[n] = *(const f32x4*)(bb + 4 * n); bl[n] = *(const f32x4*)(bb + de + 4 * n); }
; #pragma unroll
;         for (int ai = 0; ai < 2; ++ai)
; #pragma unroll
;             for (int m = 0; m < 4; ++m) { unsigned char* rowp = O + (size_t)(row0 + ai * HALF + m * 16) * ldc + cl;
;                 f32x4 a[2];
; #pragma unroll
;                 for (int n = 0; n < 2; ++n) { const f32x4 g = acc[ai][0][m][n] * ascale + bg[n], l = acc[ai][1][m][n] * ascale + bl[n];
;                     f32x4 gg, ll, ex, rc;
; #pragma unroll
;                     for (int j = 0; j < 4; ++j) { gg[j] = fminf(g[j], 7.0f); ll[j] = __builtin_amdgcn_fmed3f(l[j], -7.0f, 7.0f); }
;                     const f32x4 t = gg * (-1.702f * 1.44269504089f);
; #pragma unroll
;                     for (int j = 0; j < 4; ++j) ex[j] = __builtin_amdgcn_exp2f(t[j]);
;                     const f32x4 d = ex + 1.0f;
; #pragma unroll
;                     for (int j = 0; j < 4; ++j) rc[j] = __builtin_amdgcn_rcpf(d[j]);
;                     a[n] = (gg * rc) * (ll * oscale + oscale); }
;                 int w0 = 0, w1 = 0;
;                 w0 = __builtin_amdgcn_cvt_pk_fp8_f32(a[0][0], a[0][1], w0, false); w0 = __builtin_amdgcn_cvt_pk_fp8_f32(a[0][2], a[0][3], w0, true);
;                 w1 = __builtin_amdgcn_cvt_pk_fp8_f32(a[1][0], a[1][1], w1, false); w1 = __builtin_amdgcn_cvt_pk_fp8_f32(a[1][2], a[1][3], w1, true);
;                 u32x2 w; w.x = (unsigned)w0; w.y = (unsigned)w1; *(u32x2*)rowp = w; }
.LBB0_1389:
	v_ashrrev_i32_e32 v171, 31, v170
	v_lshl_or_b32 v20, s60, 7, v196
	v_and_b32_e32 v28, 31, v196
	s_lshl_b32 s100, s96, 8
	s_add_i32 s100, s100, 0x20800
	v_lshl_add_u32 v28, v28, 2, s100
	ds_read_b128 v[14:17], v28
	ds_read_b128 v[6:9], v28 offset:16
	ds_read_b128 v[10:13], v28 offset:128
	ds_read_b128 v[2:5], v28 offset:144
	v_ashrrev_i32_e32 v21, 31, v20
	v_lshl_add_u32 v22, s58, 8, v173
	v_ashrrev_i32_e32 v23, 31, v22
	v_lshlrev_b64 v[18:19], 11, v[22:23]
	v_mov_b32_e32 v24, v163
	v_mov_b32_e32 v25, v163
	v_lshl_add_u64 v[18:19], s[14:15], 0, v[18:19]
	v_lshl_add_u64 v[18:19], v[18:19], 0, v[20:21]
	v_or_b32_e32 v26, 16, v22
	v_ashrrev_i32_e32 v27, 31, v26
	v_readlane_b32 s37, v253, 2
	s_waitcnt lgkmcnt(0)
	v_fmamk_f32 v23, v158, 0x3b000000, v14
	v_fmamk_f32 v29, v159, 0x3b000000, v15
	v_fmamk_f32 v32, v154, 0x3b000000, v6
	v_fmamk_f32 v33, v155, 0x3b000000, v7
	v_fmamk_f32 v30, v160, 0x3b000000, v16
	v_fmamk_f32 v154, v156, 0x3b000000, v8
	v_min_f32_e32 v28, 0x40e00000, v23
	v_min_f32_e32 v29, 0x40e00000, v29
	v_min_f32_e32 v32, 0x40e00000, v32
	v_min_f32_e32 v33, 0x40e00000, v33
	v_min_f32_e32 v30, 0x40e00000, v30
	v_min_f32_e32 v154, 0x40e00000, v154
	v_fmamk_f32 v23, v150, 0x3b000000, v10
	v_fmamk_f32 v150, v151, 0x3b000000, v11
	v_fmamk_f32 v151, v152, 0x3b000000, v12
	v_fmamk_f32 v152, v153, 0x3b000000, v13
	v_mul_f32_e32 v153, 0xc01d265f, v28
	v_mul_f32_e32 v156, 0xc01d265f, v29
	v_fmamk_f32 v159, v146, 0x3b000000, v2
	v_fmamk_f32 v160, v147, 0x3b000000, v3
	v_mul_f32_e32 v170, 0xc01d265f, v32
	v_mul_f32_e32 v171, 0xc01d265f, v33
	v_fmamk_f32 v31, v161, 0x3b000000, v17
	v_fmamk_f32 v155, v157, 0x3b000000, v9
	v_mul_f32_e32 v157, 0xc01d265f, v30
	v_fmamk_f32 v161, v148, 0x3b000000, v4
	v_mul_f32_e32 v172, 0xc01d265f, v154
	v_med3_f32 v146, v23, s72, v201
	v_med3_f32 v147, v150, s72, v201
	v_med3_f32 v148, v151, s72, v201
	v_exp_f32_e32 v23, v153
	v_exp_f32_e32 v156, v156
	v_med3_f32 v150, v159, s72, v201
	v_med3_f32 v151, v160, s72, v201
	v_exp_f32_e32 v159, v170
	v_exp_f32_e32 v160, v171
	v_fmamk_f32 v162, v149, 0x3b000000, v5
	v_med3_f32 v149, v152, s72, v201
	v_exp_f32_e32 v157, v157
	v_med3_f32 v152, v161, s72, v201
	v_exp_f32_e32 v161, v172
	v_min_f32_e32 v31, 0x40e00000, v31
	v_min_f32_e32 v155, 0x40e00000, v155
	v_mul_f32_e32 v158, 0xc01d265f, v31
	v_mul_f32_e32 v174, 0xc01d265f, v155
	v_exp_f32_e32 v158, v158
	v_med3_f32 v153, v162, s72, v201
	v_exp_f32_e32 v162, v174
	v_add_f32_e32 v23, 1.0, v23
	v_add_f32_e32 v170, 1.0, v156
	v_add_f32_e32 v174, 1.0, v159
	v_add_f32_e32 v175, 1.0, v160
	v_add_f32_e32 v171, 1.0, v157
	v_add_f32_e32 v176, 1.0, v161
	v_rcp_f32_e32 v156, v23
	v_rcp_f32_e32 v157, v170
	v_rcp_f32_e32 v160, v174
	v_rcp_f32_e32 v161, v175
	v_add_f32_e32 v172, 1.0, v158
	v_add_f32_e32 v162, 1.0, v162
	v_pk_fma_f32 v[146:147], v[146:147], 4.0, 4.0 op_sel_hi:[1,0,0]
	v_pk_fma_f32 v[150:151], v[150:151], 4.0, 4.0 op_sel_hi:[1,0,0]
	v_rcp_f32_e32 v158, v171
	v_rcp_f32_e32 v159, v172
	v_rcp_f32_e32 v170, v176
	v_rcp_f32_e32 v171, v162
	v_pk_mul_f32 v[28:29], v[28:29], v[156:157]
	v_pk_mul_f32 v[32:33], v[32:33], v[160:161]
	v_pk_mul_f32 v[28:29], v[146:147], v[28:29]
	v_pk_mul_f32 v[32:33], v[150:151], v[32:33]
	v_cvt_pk_fp8_f32 v24, v28, v29
	v_cvt_pk_fp8_f32 v25, v32, v33
	v_pk_fma_f32 v[148:149], v[148:149], 4.0, 4.0 op_sel_hi:[1,0,0]
	v_pk_fma_f32 v[152:153], v[152:153], 4.0, 4.0 op_sel_hi:[1,0,0]
	v_pk_mul_f32 v[30:31], v[30:31], v[158:159]
	v_pk_mul_f32 v[154:155], v[154:155], v[170:171]
	v_pk_mul_f32 v[28:29], v[148:149], v[30:31]
	v_pk_mul_f32 v[30:31], v[152:153], v[154:155]
	v_cvt_pk_fp8_f32 v24, v28, v29 op_sel:[0,0,1]
	v_cvt_pk_fp8_f32 v25, v30, v31 op_sel:[0,0,1]
	v_fmamk_f32 v23, v142, 0x3b000000, v14
	global_store_dwordx2 v[18:19], v[24:25], off
	v_min_f32_e32 v24, 0x40e00000, v23
	v_fmamk_f32 v23, v138, 0x3b000000, v10
	v_med3_f32 v28, v23, s72, v201
	v_fmamk_f32 v23, v143, 0x3b000000, v15
	v_min_f32_e32 v25, 0x40e00000, v23
	v_fmamk_f32 v23, v139, 0x3b000000, v11
	v_med3_f32 v29, v23, s72, v201
	v_fmamk_f32 v23, v144, 0x3b000000, v16
	v_min_f32_e32 v30, 0x40e00000, v23
	v_fmamk_f32 v23, v140, 0x3b000000, v12
	v_med3_f32 v32, v23, s72, v201
	v_fmamk_f32 v23, v145, 0x3b000000, v17
	v_min_f32_e32 v31, 0x40e00000, v23
	v_mul_f32_e32 v23, 0xc01d265f, v24
	v_exp_f32_e32 v23, v23
	v_mul_f32_e32 v33, 0xc01d265f, v25
	v_exp_f32_e32 v33, v33
	v_mul_f32_e32 v138, 0xc01d265f, v30
	v_exp_f32_e32 v140, v138
	v_mul_f32_e32 v138, 0xc01d265f, v31
	v_exp_f32_e32 v143, v138
	v_add_f32_e32 v23, 1.0, v23
	v_rcp_f32_e32 v138, v23
	v_add_f32_e32 v23, 1.0, v33
	v_rcp_f32_e32 v139, v23
	v_add_f32_e32 v23, 1.0, v140
	v_rcp_f32_e32 v142, v23
	v_add_f32_e32 v23, 1.0, v143
	v_rcp_f32_e32 v143, v23
	v_fmamk_f32 v23, v141, 0x3b000000, v13
	v_med3_f32 v33, v23, s72, v201
	v_pk_mul_f32 v[24:25], v[24:25], v[138:139]
	v_pk_fma_f32 v[28:29], v[28:29], 4.0, 4.0 op_sel_hi:[1,0,0]
	v_fmamk_f32 v23, v134, 0x3b000000, v6
	v_pk_mul_f32 v[30:31], v[30:31], v[142:143]
	v_pk_fma_f32 v[32:33], v[32:33], 4.0, 4.0 op_sel_hi:[1,0,0]
	v_pk_mul_f32 v[24:25], v[28:29], v[24:25]
	v_min_f32_e32 v28, 0x40e00000, v23
	v_fmamk_f32 v23, v130, 0x3b000000, v2
	v_pk_mul_f32 v[30:31], v[32:33], v[30:31]
	v_med3_f32 v32, v23, s72, v201
	v_fmamk_f32 v23, v135, 0x3b000000, v7
	v_min_f32_e32 v29, 0x40e00000, v23
	v_fmamk_f32 v23, v131, 0x3b000000, v3
	v_med3_f32 v33, v23, s72, v201
	v_fmamk_f32 v23, v136, 0x3b000000, v8
	v_min_f32_e32 v130, 0x40e00000, v23
	v_fmamk_f32 v23, v132, 0x3b000000, v4
	v_med3_f32 v132, v23, s72, v201
	v_fmamk_f32 v23, v137, 0x3b000000, v9
	v_min_f32_e32 v131, 0x40e00000, v23
	v_mul_f32_e32 v23, 0xc01d265f, v28
;     __device__ __forceinline__ void operator()(const f32x4 (&acc)[2][2][4][2], const Unit& u, int wr, int wc, int fr, int fq) const {
;     ...
;         for (int ai = 0; ai < 2; ++ai)
; #pragma unroll
;             for (int m = 0; m < 4; ++m) { unsigned char* rowp = O + (size_t)(row0 + ai * HALF + m * 16) * ldc + cl;
;                 f32x4 a[2];
; #pragma unroll
;                 for (int n = 0; n < 2; ++n) { const f32x4 g = acc[ai][0][m][n] * ascale + bg[n], l = acc[ai][1][m][n] * ascale + bl[n];
;                     f32x4 gg, ll, ex, rc;
; #pragma unroll
;                     for (int j = 0; j < 4; ++j) { gg[j] = fminf(g[j], 7.0f); ll[j] = __builtin_amdgcn_fmed3f(l[j], -7.0f, 7.0f); }
;                     const f32x4 t = gg * (-1.702f * 1.44269504089f);
; #pragma unroll
;                     for (int j = 0; j < 4; ++j) ex[j] = __builtin_amdgcn_exp2f(t[j]);
;                     const f32x4 d = ex + 1.0f;
; #pragma unroll
;                     for (int j = 0; j < 4; ++j) rc[j] = __builtin_amdgcn_rcpf(d[j]);
;                     a[n] = (gg * rc) * (ll * oscale + oscale); }
;                 int w0 = 0, w1 = 0;
;                 w0 = __builtin_amdgcn_cvt_pk_fp8_f32(a[0][0], a[0][1], w0, false); w0 = __builtin_amdgcn_cvt_pk_fp8_f32(a[0][2], a[0][3], w0, true);
;                 w1 = __builtin_amdgcn_cvt_pk_fp8_f32(a[1][0], a[1][1], w1, false); w1 = __builtin_amdgcn_cvt_pk_fp8_f32(a[1][2], a[1][3], w1, true);
;                 u32x2 w; w.x = (unsigned)w0; w.y = (unsigned)w1; *(u32x2*)rowp = w; }
	v_exp_f32_e32 v23, v23
	v_mul_f32_e32 v134, 0xc01d265f, v29
	v_exp_f32_e32 v135, v134
	v_mul_f32_e32 v134, 0xc01d265f, v130
	v_exp_f32_e32 v136, v134
	v_mul_f32_e32 v134, 0xc01d265f, v131
	v_add_f32_e32 v23, 1.0, v23
	v_exp_f32_e32 v137, v134
	v_rcp_f32_e32 v134, v23
	v_add_f32_e32 v23, 1.0, v135
	v_rcp_f32_e32 v135, v23
	v_add_f32_e32 v23, 1.0, v136
	v_rcp_f32_e32 v136, v23
	v_add_f32_e32 v23, 1.0, v137
	v_rcp_f32_e32 v137, v23
	v_pk_mul_f32 v[28:29], v[28:29], v[134:135]
	v_pk_fma_f32 v[32:33], v[32:33], 4.0, 4.0 op_sel_hi:[1,0,0]
	v_fmamk_f32 v23, v133, 0x3b000000, v5
	v_pk_mul_f32 v[28:29], v[32:33], v[28:29]
	v_mov_b32_e32 v33, v163
	v_mov_b32_e32 v32, v163
	v_cvt_pk_fp8_f32 v33, v28, v29
	v_med3_f32 v133, v23, s72, v201
	v_cvt_pk_fp8_f32 v32, v24, v25
	v_pk_mul_f32 v[130:131], v[130:131], v[136:137]
	v_pk_fma_f32 v[24:25], v[132:133], 4.0, 4.0 op_sel_hi:[1,0,0]
	v_fmamk_f32 v23, v126, 0x3b000000, v14
	v_pk_mul_f32 v[24:25], v[24:25], v[130:131]
	v_cvt_pk_fp8_f32 v32, v30, v31 op_sel:[0,0,1]
	v_cvt_pk_fp8_f32 v33, v24, v25 op_sel:[0,0,1]
	v_lshlrev_b64 v[24:25], 11, v[26:27]
	v_min_f32_e32 v26, 0x40e00000, v23
	v_fmamk_f32 v23, v122, 0x3b000000, v10
	v_med3_f32 v28, v23, s72, v201
	v_fmamk_f32 v23, v127, 0x3b000000, v15
	v_min_f32_e32 v27, 0x40e00000, v23
	v_fmamk_f32 v23, v123, 0x3b000000, v11
	v_lshl_add_u64 v[24:25], s[14:15], 0, v[24:25]
	v_med3_f32 v29, v23, s72, v201
	v_fmamk_f32 v23, v128, 0x3b000000, v16
	v_lshl_add_u64 v[24:25], v[24:25], 0, v[20:21]
	v_min_f32_e32 v30, 0x40e00000, v23
	v_fmamk_f32 v23, v124, 0x3b000000, v12
	global_store_dwordx2 v[24:25], v[32:33], off
	v_med3_f32 v32, v23, s72, v201
	v_fmamk_f32 v23, v129, 0x3b000000, v17
	v_min_f32_e32 v31, 0x40e00000, v23
	v_mul_f32_e32 v23, 0xc01d265f, v26
	v_exp_f32_e32 v23, v23
	v_mul_f32_e32 v33, 0xc01d265f, v27
	v_exp_f32_e32 v33, v33
	v_mul_f32_e32 v122, 0xc01d265f, v30
	v_exp_f32_e32 v124, v122
	v_mul_f32_e32 v122, 0xc01d265f, v31
	v_exp_f32_e32 v127, v122
	v_add_f32_e32 v23, 1.0, v23
	v_rcp_f32_e32 v122, v23
	v_add_f32_e32 v23, 1.0, v33
	v_rcp_f32_e32 v123, v23
	v_add_f32_e32 v23, 1.0, v124
	v_rcp_f32_e32 v126, v23
	v_add_f32_e32 v23, 1.0, v127
	v_rcp_f32_e32 v127, v23
	v_fmamk_f32 v23, v125, 0x3b000000, v13
	v_med3_f32 v33, v23, s72, v201
	v_pk_mul_f32 v[26:27], v[26:27], v[122:123]
	v_pk_fma_f32 v[28:29], v[28:29], 4.0, 4.0 op_sel_hi:[1,0,0]
	v_fmamk_f32 v23, v118, 0x3b000000, v6
	v_pk_mul_f32 v[30:31], v[30:31], v[126:127]
	v_pk_fma_f32 v[32:33], v[32:33], 4.0, 4.0 op_sel_hi:[1,0,0]
	v_pk_mul_f32 v[26:27], v[28:29], v[26:27]
	v_min_f32_e32 v28, 0x40e00000, v23
	v_fmamk_f32 v23, v114, 0x3b000000, v2
	v_pk_mul_f32 v[30:31], v[32:33], v[30:31]
	v_med3_f32 v32, v23, s72, v201
	v_fmamk_f32 v23, v119, 0x3b000000, v7
	v_min_f32_e32 v29, 0x40e00000, v23
	v_fmamk_f32 v23, v115, 0x3b000000, v3
	v_med3_f32 v33, v23, s72, v201
	v_fmamk_f32 v23, v120, 0x3b000000, v8
	v_min_f32_e32 v114, 0x40e00000, v23
	v_fmamk_f32 v23, v116, 0x3b000000, v4
	v_med3_f32 v116, v23, s72, v201
	v_fmamk_f32 v23, v121, 0x3b000000, v9
	v_min_f32_e32 v115, 0x40e00000, v23
	v_mul_f32_e32 v23, 0xc01d265f, v28
	v_exp_f32_e32 v23, v23
	v_mul_f32_e32 v118, 0xc01d265f, v29
	v_exp_f32_e32 v119, v118
	v_mul_f32_e32 v118, 0xc01d265f, v114
	v_exp_f32_e32 v120, v118
	v_mul_f32_e32 v118, 0xc01d265f, v115
	v_add_f32_e32 v23, 1.0, v23
	v_exp_f32_e32 v121, v118
	v_rcp_f32_e32 v118, v23
	v_add_f32_e32 v23, 1.0, v119
	v_rcp_f32_e32 v119, v23
	v_add_f32_e32 v23, 1.0, v120
	v_rcp_f32_e32 v120, v23
	v_add_f32_e32 v23, 1.0, v121
	v_rcp_f32_e32 v121, v23
	v_pk_mul_f32 v[28:29], v[28:29], v[118:119]
	v_pk_fma_f32 v[32:33], v[32:33], 4.0, 4.0 op_sel_hi:[1,0,0]
	v_fmamk_f32 v23, v117, 0x3b000000, v5
	v_pk_mul_f32 v[28:29], v[32:33], v[28:29]
	v_mov_b32_e32 v32, v163
	v_mov_b32_e32 v33, v163
	v_cvt_pk_fp8_f32 v32, v26, v27
	v_cvt_pk_fp8_f32 v33, v28, v29
	v_med3_f32 v117, v23, s72, v201
	v_pk_mul_f32 v[114:115], v[114:115], v[120:121]
	v_pk_fma_f32 v[26:27], v[116:117], 4.0, 4.0 op_sel_hi:[1,0,0]
	v_or_b32_e32 v24, 32, v22
	v_pk_mul_f32 v[26:27], v[26:27], v[114:115]
	v_ashrrev_i32_e32 v25, 31, v24
	v_cvt_pk_fp8_f32 v32, v30, v31 op_sel:[0,0,1]
	v_cvt_pk_fp8_f32 v33, v26, v27 op_sel:[0,0,1]
	v_lshlrev_b64 v[24:25], 11, v[24:25]
	v_lshl_add_u64 v[24:25], s[14:15], 0, v[24:25]
	v_lshl_add_u64 v[24:25], v[24:25], 0, v[20:21]
	global_store_dwordx2 v[24:25], v[32:33], off
	v_fmamk_f32 v24, v110, 0x3b000000, v14
	v_fmamk_f32 v25, v106, 0x3b000000, v10
	v_min_f32_e32 v24, 0x40e00000, v24
	v_med3_f32 v26, v25, s72, v201
	v_fmamk_f32 v25, v111, 0x3b000000, v15
	v_min_f32_e32 v25, 0x40e00000, v25
	v_fmamk_f32 v28, v112, 0x3b000000, v16
	v_fmamk_f32 v29, v108, 0x3b000000, v12
	v_mul_f32_e32 v31, 0xc01d265f, v24
	v_min_f32_e32 v28, 0x40e00000, v28
	v_med3_f32 v30, v29, s72, v201
	v_fmamk_f32 v29, v113, 0x3b000000, v17
	v_exp_f32_e32 v31, v31
	v_mul_f32_e32 v32, 0xc01d265f, v25
	v_min_f32_e32 v29, 0x40e00000, v29
	v_exp_f32_e32 v33, v32
	v_mul_f32_e32 v32, 0xc01d265f, v28
	v_exp_f32_e32 v106, v32
	v_mul_f32_e32 v32, 0xc01d265f, v29
	v_fmamk_f32 v27, v107, 0x3b000000, v11
	v_exp_f32_e32 v107, v32
	v_add_f32_e32 v31, 1.0, v31
	v_rcp_f32_e32 v32, v31
	v_add_f32_e32 v31, 1.0, v33
	v_rcp_f32_e32 v33, v31
	v_add_f32_e32 v31, 1.0, v106
	v_rcp_f32_e32 v106, v31
	v_add_f32_e32 v31, 1.0, v107
	v_rcp_f32_e32 v107, v31
	v_med3_f32 v27, v27, s72, v201
	v_fmamk_f32 v31, v109, 0x3b000000, v13
	v_med3_f32 v31, v31, s72, v201
	v_pk_mul_f32 v[24:25], v[24:25], v[32:33]
	v_pk_fma_f32 v[26:27], v[26:27], 4.0, 4.0 op_sel_hi:[1,0,0]
	v_pk_mul_f32 v[28:29], v[28:29], v[106:107]
	v_pk_fma_f32 v[30:31], v[30:31], 4.0, 4.0 op_sel_hi:[1,0,0]
;     __device__ __forceinline__ void operator()(const f32x4 (&acc)[2][2][4][2], const Unit& u, int wr, int wc, int fr, int fq) const {
;     ...
;         for (int ai = 0; ai < 2; ++ai)
; #pragma unroll
;             for (int m = 0; m < 4; ++m) { unsigned char* rowp = O + (size_t)(row0 + ai * HALF + m * 16) * ldc + cl;
;                 f32x4 a[2];
; #pragma unroll
;                 for (int n = 0; n < 2; ++n) { const f32x4 g = acc[ai][0][m][n] * ascale + bg[n], l = acc[ai][1][m][n] * ascale + bl[n];
;                     f32x4 gg, ll, ex, rc;
; #pragma unroll
;                     for (int j = 0; j < 4; ++j) { gg[j] = fminf(g[j], 7.0f); ll[j] = __builtin_amdgcn_fmed3f(l[j], -7.0f, 7.0f); }
;                     const f32x4 t = gg * (-1.702f * 1.44269504089f);
; #pragma unroll
;                     for (int j = 0; j < 4; ++j) ex[j] = __builtin_amdgcn_exp2f(t[j]);
;                     const f32x4 d = ex + 1.0f;
; #pragma unroll
;                     for (int j = 0; j < 4; ++j) rc[j] = __builtin_amdgcn_rcpf(d[j]);
;                     a[n] = (gg * rc) * (ll * oscale + oscale); }
;                 int w0 = 0, w1 = 0;
;                 w0 = __builtin_amdgcn_cvt_pk_fp8_f32(a[0][0], a[0][1], w0, false); w0 = __builtin_amdgcn_cvt_pk_fp8_f32(a[0][2], a[0][3], w0, true);
;                 w1 = __builtin_amdgcn_cvt_pk_fp8_f32(a[1][0], a[1][1], w1, false); w1 = __builtin_amdgcn_cvt_pk_fp8_f32(a[1][2], a[1][3], w1, true);
;                 u32x2 w; w.x = (unsigned)w0; w.y = (unsigned)w1; *(u32x2*)rowp = w; }
	v_pk_mul_f32 v[24:25], v[26:27], v[24:25]
	v_fmamk_f32 v26, v102, 0x3b000000, v6
	v_fmamk_f32 v27, v98, 0x3b000000, v2
	v_pk_mul_f32 v[28:29], v[30:31], v[28:29]
	v_min_f32_e32 v26, 0x40e00000, v26
	v_med3_f32 v30, v27, s72, v201
	v_fmamk_f32 v27, v103, 0x3b000000, v7
	v_min_f32_e32 v27, 0x40e00000, v27
	v_fmamk_f32 v31, v99, 0x3b000000, v3
	v_mul_f32_e32 v99, 0xc01d265f, v26
	v_fmamk_f32 v33, v100, 0x3b000000, v4
	v_exp_f32_e32 v99, v99
	v_mul_f32_e32 v100, 0xc01d265f, v27
	v_fmamk_f32 v32, v104, 0x3b000000, v8
	v_exp_f32_e32 v100, v100
	v_min_f32_e32 v32, 0x40e00000, v32
	v_med3_f32 v98, v33, s72, v201
	v_fmamk_f32 v33, v105, 0x3b000000, v9
	v_min_f32_e32 v33, 0x40e00000, v33
	v_mul_f32_e32 v102, 0xc01d265f, v32
	v_exp_f32_e32 v104, v102
	v_mul_f32_e32 v102, 0xc01d265f, v33
	v_add_f32_e32 v99, 1.0, v99
	v_exp_f32_e32 v105, v102
	v_rcp_f32_e32 v102, v99
	v_add_f32_e32 v99, 1.0, v100
	v_rcp_f32_e32 v103, v99
	v_add_f32_e32 v99, 1.0, v104
	v_med3_f32 v31, v31, s72, v201
	v_rcp_f32_e32 v104, v99
	v_add_f32_e32 v99, 1.0, v105
	v_rcp_f32_e32 v105, v99
	v_pk_mul_f32 v[26:27], v[26:27], v[102:103]
	v_pk_fma_f32 v[30:31], v[30:31], 4.0, 4.0 op_sel_hi:[1,0,0]
	v_fmamk_f32 v99, v101, 0x3b000000, v5
	v_pk_mul_f32 v[26:27], v[30:31], v[26:27]
	v_mov_b32_e32 v30, v163
	v_mov_b32_e32 v31, v163
	v_cvt_pk_fp8_f32 v30, v24, v25
	v_cvt_pk_fp8_f32 v31, v26, v27
	v_med3_f32 v99, v99, s72, v201
	v_pk_mul_f32 v[32:33], v[32:33], v[104:105]
	v_pk_fma_f32 v[24:25], v[98:99], 4.0, 4.0 op_sel_hi:[1,0,0]
	v_or_b32_e32 v22, 48, v22
	v_pk_mul_f32 v[24:25], v[24:25], v[32:33]
	v_ashrrev_i32_e32 v23, 31, v22
	v_cvt_pk_fp8_f32 v30, v28, v29 op_sel:[0,0,1]
	v_cvt_pk_fp8_f32 v31, v24, v25 op_sel:[0,0,1]
	v_lshlrev_b64 v[22:23], 11, v[22:23]
	v_lshl_add_u64 v[22:23], s[14:15], 0, v[22:23]
	v_lshl_add_u64 v[20:21], v[22:23], 0, v[20:21]
	global_store_dwordx2 v[20:21], v[30:31], off
	v_fmamk_f32 v20, v94, 0x3b000000, v14
	v_fmamk_f32 v21, v90, 0x3b000000, v10
	v_min_f32_e32 v20, 0x40e00000, v20
	v_med3_f32 v22, v21, s72, v201
	v_fmamk_f32 v21, v95, 0x3b000000, v15
	v_min_f32_e32 v21, 0x40e00000, v21
	v_fmamk_f32 v24, v96, 0x3b000000, v16
	v_fmamk_f32 v25, v92, 0x3b000000, v12
	v_mul_f32_e32 v27, 0xc01d265f, v20
	v_min_f32_e32 v24, 0x40e00000, v24
	v_med3_f32 v26, v25, s72, v201
	v_fmamk_f32 v25, v97, 0x3b000000, v17
	v_exp_f32_e32 v27, v27
	v_mul_f32_e32 v28, 0xc01d265f, v21
	v_min_f32_e32 v25, 0x40e00000, v25
	v_exp_f32_e32 v29, v28
	v_mul_f32_e32 v28, 0xc01d265f, v24
	v_exp_f32_e32 v30, v28
	v_mul_f32_e32 v28, 0xc01d265f, v25
	v_exp_f32_e32 v31, v28
	v_add_f32_e32 v27, 1.0, v27
	v_rcp_f32_e32 v28, v27
	v_add_f32_e32 v27, 1.0, v29
	v_rcp_f32_e32 v29, v27
	v_add_f32_e32 v27, 1.0, v30
	v_rcp_f32_e32 v30, v27
	v_add_f32_e32 v27, 1.0, v31
	v_rcp_f32_e32 v31, v27
	v_fmamk_f32 v23, v91, 0x3b000000, v11
	v_med3_f32 v23, v23, s72, v201
	v_fmamk_f32 v27, v93, 0x3b000000, v13
	v_med3_f32 v27, v27, s72, v201
	v_pk_mul_f32 v[20:21], v[20:21], v[28:29]
	v_pk_fma_f32 v[22:23], v[22:23], 4.0, 4.0 op_sel_hi:[1,0,0]
	v_pk_mul_f32 v[24:25], v[24:25], v[30:31]
	v_pk_fma_f32 v[26:27], v[26:27], 4.0, 4.0 op_sel_hi:[1,0,0]
	v_pk_mul_f32 v[20:21], v[22:23], v[20:21]
	v_fmamk_f32 v22, v86, 0x3b000000, v6
	v_fmamk_f32 v23, v82, 0x3b000000, v2
	v_pk_mul_f32 v[24:25], v[26:27], v[24:25]
	v_min_f32_e32 v22, 0x40e00000, v22
	v_med3_f32 v26, v23, s72, v201
	v_fmamk_f32 v23, v87, 0x3b000000, v7
	v_min_f32_e32 v23, 0x40e00000, v23
	v_mul_f32_e32 v31, 0xc01d265f, v22
	v_exp_f32_e32 v31, v31
	v_mul_f32_e32 v32, 0xc01d265f, v23
	v_fmamk_f32 v28, v88, 0x3b000000, v8
	v_fmamk_f32 v29, v84, 0x3b000000, v4
	v_exp_f32_e32 v33, v32
	v_min_f32_e32 v28, 0x40e00000, v28
	v_med3_f32 v30, v29, s72, v201
	v_fmamk_f32 v29, v89, 0x3b000000, v9
	v_min_f32_e32 v29, 0x40e00000, v29
	v_mul_f32_e32 v32, 0xc01d265f, v28
	v_exp_f32_e32 v82, v32
	v_mul_f32_e32 v32, 0xc01d265f, v29
	v_add_f32_e32 v31, 1.0, v31
	v_fmamk_f32 v27, v83, 0x3b000000, v3
	v_exp_f32_e32 v83, v32
	v_rcp_f32_e32 v32, v31
	v_add_f32_e32 v31, 1.0, v33
	v_rcp_f32_e32 v33, v31
	v_add_f32_e32 v31, 1.0, v82
	v_med3_f32 v27, v27, s72, v201
	v_rcp_f32_e32 v82, v31
	v_add_f32_e32 v31, 1.0, v83
	v_rcp_f32_e32 v83, v31
	v_pk_mul_f32 v[22:23], v[22:23], v[32:33]
	v_pk_fma_f32 v[26:27], v[26:27], 4.0, 4.0 op_sel_hi:[1,0,0]
	v_fmamk_f32 v31, v85, 0x3b000000, v5
	v_pk_mul_f32 v[22:23], v[26:27], v[22:23]
	v_mov_b32_e32 v26, v163
	v_mov_b32_e32 v27, v163
	v_cvt_pk_fp8_f32 v26, v20, v21
	v_cvt_pk_fp8_f32 v27, v22, v23
	v_med3_f32 v31, v31, s72, v201
	v_pk_mul_f32 v[28:29], v[28:29], v[82:83]
	v_pk_fma_f32 v[20:21], v[30:31], 4.0, 4.0 op_sel_hi:[1,0,0]
	v_cvt_pk_fp8_f32 v26, v24, v25 op_sel:[0,0,1]
	v_pk_mul_f32 v[20:21], v[20:21], v[28:29]
	v_fmamk_f32 v24, v80, 0x3b000000, v16
	v_cvt_pk_fp8_f32 v27, v20, v21 op_sel:[0,0,1]
	v_add_co_u32_e32 v20, vcc, s73, v18
	v_fmamk_f32 v25, v76, 0x3b000000, v12
	s_nop 0
	v_addc_co_u32_e32 v21, vcc, 0, v19, vcc
	global_store_dwordx2 v[20:21], v[26:27], off
	v_fmamk_f32 v20, v78, 0x3b000000, v14
	v_fmamk_f32 v21, v74, 0x3b000000, v10
	v_min_f32_e32 v20, 0x40e00000, v20
	v_med3_f32 v22, v21, s72, v201
	v_fmamk_f32 v21, v79, 0x3b000000, v15
	v_min_f32_e32 v21, 0x40e00000, v21
	v_mul_f32_e32 v27, 0xc01d265f, v20
	v_min_f32_e32 v24, 0x40e00000, v24
	v_med3_f32 v26, v25, s72, v201
	v_fmamk_f32 v25, v81, 0x3b000000, v17
	v_exp_f32_e32 v27, v27
	v_mul_f32_e32 v28, 0xc01d265f, v21
	v_min_f32_e32 v25, 0x40e00000, v25
	v_exp_f32_e32 v29, v28
	v_mul_f32_e32 v28, 0xc01d265f, v24
	v_exp_f32_e32 v30, v28
	v_mul_f32_e32 v28, 0xc01d265f, v25
	v_exp_f32_e32 v31, v28
	v_add_f32_e32 v27, 1.0, v27
	v_rcp_f32_e32 v28, v27
	v_add_f32_e32 v27, 1.0, v29
;     __device__ __forceinline__ void operator()(const f32x4 (&acc)[2][2][4][2], const Unit& u, int wr, int wc, int fr, int fq) const {
;     ...
;         for (int ai = 0; ai < 2; ++ai)
; #pragma unroll
;             for (int m = 0; m < 4; ++m) { unsigned char* rowp = O + (size_t)(row0 + ai * HALF + m * 16) * ldc + cl;
;                 f32x4 a[2];
; #pragma unroll
;                 for (int n = 0; n < 2; ++n) { const f32x4 g = acc[ai][0][m][n] * ascale + bg[n], l = acc[ai][1][m][n] * ascale + bl[n];
;                     f32x4 gg, ll, ex, rc;
; #pragma unroll
;                     for (int j = 0; j < 4; ++j) { gg[j] = fminf(g[j], 7.0f); ll[j] = __builtin_amdgcn_fmed3f(l[j], -7.0f, 7.0f); }
;                     const f32x4 t = gg * (-1.702f * 1.44269504089f);
; #pragma unroll
;                     for (int j = 0; j < 4; ++j) ex[j] = __builtin_amdgcn_exp2f(t[j]);
;                     const f32x4 d = ex + 1.0f;
; #pragma unroll
;                     for (int j = 0; j < 4; ++j) rc[j] = __builtin_amdgcn_rcpf(d[j]);
;                     a[n] = (gg * rc) * (ll * oscale + oscale); }
;                 int w0 = 0, w1 = 0;
;                 w0 = __builtin_amdgcn_cvt_pk_fp8_f32(a[0][0], a[0][1], w0, false); w0 = __builtin_amdgcn_cvt_pk_fp8_f32(a[0][2], a[0][3], w0, true);
;                 w1 = __builtin_amdgcn_cvt_pk_fp8_f32(a[1][0], a[1][1], w1, false); w1 = __builtin_amdgcn_cvt_pk_fp8_f32(a[1][2], a[1][3], w1, true);
;                 u32x2 w; w.x = (unsigned)w0; w.y = (unsigned)w1; *(u32x2*)rowp = w; }
	v_rcp_f32_e32 v29, v27
	v_add_f32_e32 v27, 1.0, v30
	v_rcp_f32_e32 v30, v27
	v_add_f32_e32 v27, 1.0, v31
	v_rcp_f32_e32 v31, v27
	v_fmamk_f32 v23, v75, 0x3b000000, v11
	v_med3_f32 v23, v23, s72, v201
	v_fmamk_f32 v27, v77, 0x3b000000, v13
	v_med3_f32 v27, v27, s72, v201
	v_pk_mul_f32 v[20:21], v[20:21], v[28:29]
	v_pk_fma_f32 v[22:23], v[22:23], 4.0, 4.0 op_sel_hi:[1,0,0]
	v_pk_mul_f32 v[24:25], v[24:25], v[30:31]
	v_pk_fma_f32 v[26:27], v[26:27], 4.0, 4.0 op_sel_hi:[1,0,0]
	v_pk_mul_f32 v[20:21], v[22:23], v[20:21]
	v_fmamk_f32 v22, v70, 0x3b000000, v6
	v_fmamk_f32 v23, v66, 0x3b000000, v2
	v_pk_mul_f32 v[24:25], v[26:27], v[24:25]
	v_min_f32_e32 v22, 0x40e00000, v22
	v_med3_f32 v26, v23, s72, v201
	v_fmamk_f32 v23, v71, 0x3b000000, v7
	v_min_f32_e32 v23, 0x40e00000, v23
	v_mul_f32_e32 v31, 0xc01d265f, v22
	v_exp_f32_e32 v31, v31
	v_mul_f32_e32 v32, 0xc01d265f, v23
	v_fmamk_f32 v28, v72, 0x3b000000, v8
	v_fmamk_f32 v29, v68, 0x3b000000, v4
	v_exp_f32_e32 v33, v32
	v_min_f32_e32 v28, 0x40e00000, v28
	v_med3_f32 v30, v29, s72, v201
	v_fmamk_f32 v29, v73, 0x3b000000, v9
	v_min_f32_e32 v29, 0x40e00000, v29
	v_mul_f32_e32 v32, 0xc01d265f, v28
	v_exp_f32_e32 v66, v32
	v_mul_f32_e32 v32, 0xc01d265f, v29
	v_add_f32_e32 v31, 1.0, v31
	v_fmamk_f32 v27, v67, 0x3b000000, v3
	v_exp_f32_e32 v67, v32
	v_rcp_f32_e32 v32, v31
	v_add_f32_e32 v31, 1.0, v33
	v_rcp_f32_e32 v33, v31
	v_add_f32_e32 v31, 1.0, v66
	v_med3_f32 v27, v27, s72, v201
	v_rcp_f32_e32 v66, v31
	v_add_f32_e32 v31, 1.0, v67
	v_rcp_f32_e32 v67, v31
	v_pk_mul_f32 v[22:23], v[22:23], v[32:33]
	v_pk_fma_f32 v[26:27], v[26:27], 4.0, 4.0 op_sel_hi:[1,0,0]
	v_fmamk_f32 v31, v69, 0x3b000000, v5
	v_pk_mul_f32 v[22:23], v[26:27], v[22:23]
	v_mov_b32_e32 v26, v163
	v_mov_b32_e32 v27, v163
	v_cvt_pk_fp8_f32 v26, v20, v21
	v_cvt_pk_fp8_f32 v27, v22, v23
	v_med3_f32 v31, v31, s72, v201
	v_pk_mul_f32 v[28:29], v[28:29], v[66:67]
	v_pk_fma_f32 v[20:21], v[30:31], 4.0, 4.0 op_sel_hi:[1,0,0]
	v_cvt_pk_fp8_f32 v26, v24, v25 op_sel:[0,0,1]
	v_pk_mul_f32 v[20:21], v[20:21], v[28:29]
	v_fmamk_f32 v24, v64, 0x3b000000, v16
	v_cvt_pk_fp8_f32 v27, v20, v21 op_sel:[0,0,1]
	v_add_co_u32_e32 v20, vcc, s74, v18
	v_fmamk_f32 v25, v60, 0x3b000000, v12
	s_nop 0
	v_addc_co_u32_e32 v21, vcc, 0, v19, vcc
	global_store_dwordx2 v[20:21], v[26:27], off
	v_fmamk_f32 v20, v62, 0x3b000000, v14
	v_fmamk_f32 v21, v58, 0x3b000000, v10
	v_min_f32_e32 v20, 0x40e00000, v20
	v_med3_f32 v22, v21, s72, v201
	v_fmamk_f32 v21, v63, 0x3b000000, v15
	v_min_f32_e32 v21, 0x40e00000, v21
	v_mul_f32_e32 v27, 0xc01d265f, v20
	v_min_f32_e32 v24, 0x40e00000, v24
	v_med3_f32 v26, v25, s72, v201
	v_fmamk_f32 v25, v65, 0x3b000000, v17
	v_exp_f32_e32 v27, v27
	v_mul_f32_e32 v28, 0xc01d265f, v21
	v_min_f32_e32 v25, 0x40e00000, v25
	v_exp_f32_e32 v29, v28
	v_mul_f32_e32 v28, 0xc01d265f, v24
	v_exp_f32_e32 v30, v28
	v_mul_f32_e32 v28, 0xc01d265f, v25
	v_exp_f32_e32 v31, v28
	v_add_f32_e32 v27, 1.0, v27
	v_rcp_f32_e32 v28, v27
	v_add_f32_e32 v27, 1.0, v29
	v_rcp_f32_e32 v29, v27
	v_add_f32_e32 v27, 1.0, v30
	v_rcp_f32_e32 v30, v27
	v_add_f32_e32 v27, 1.0, v31
	v_rcp_f32_e32 v31, v27
	v_fmamk_f32 v23, v59, 0x3b000000, v11
	v_med3_f32 v23, v23, s72, v201
	v_fmamk_f32 v27, v61, 0x3b000000, v13
	v_med3_f32 v27, v27, s72, v201
	v_pk_mul_f32 v[20:21], v[20:21], v[28:29]
	v_pk_fma_f32 v[22:23], v[22:23], 4.0, 4.0 op_sel_hi:[1,0,0]
	v_pk_mul_f32 v[24:25], v[24:25], v[30:31]
	v_pk_fma_f32 v[26:27], v[26:27], 4.0, 4.0 op_sel_hi:[1,0,0]
	v_pk_mul_f32 v[20:21], v[22:23], v[20:21]
	v_fmamk_f32 v22, v54, 0x3b000000, v6
	v_fmamk_f32 v23, v50, 0x3b000000, v2
	v_pk_mul_f32 v[24:25], v[26:27], v[24:25]
	v_min_f32_e32 v22, 0x40e00000, v22
	v_med3_f32 v26, v23, s72, v201
	v_fmamk_f32 v23, v55, 0x3b000000, v7
	v_min_f32_e32 v23, 0x40e00000, v23
	v_mul_f32_e32 v31, 0xc01d265f, v22
	v_exp_f32_e32 v31, v31
	v_mul_f32_e32 v32, 0xc01d265f, v23
	v_fmamk_f32 v28, v56, 0x3b000000, v8
	v_fmamk_f32 v29, v52, 0x3b000000, v4
	v_exp_f32_e32 v33, v32
	v_min_f32_e32 v28, 0x40e00000, v28
	v_med3_f32 v30, v29, s72, v201
	v_fmamk_f32 v29, v57, 0x3b000000, v9
	v_min_f32_e32 v29, 0x40e00000, v29
	v_mul_f32_e32 v32, 0xc01d265f, v28
; #define PG8_BAR __builtin_amdgcn_s_barrier()
;     __device__ __forceinline__ void operator()(const f32x4 (&acc)[2][2][4][2], const Unit& u, int wr, int wc, int fr, int fq) const {
;     ...
;         for (int ai = 0; ai < 2; ++ai)
; #pragma unroll
;             for (int m = 0; m < 4; ++m) { unsigned char* rowp = O + (size_t)(row0 + ai * HALF + m * 16) * ldc + cl;
;                 f32x4 a[2];
; #pragma unroll
;                 for (int n = 0; n < 2; ++n) { const f32x4 g = acc[ai][0][m][n] * ascale + bg[n], l = acc[ai][1][m][n] * ascale + bl[n];
;                     f32x4 gg, ll, ex, rc;
; #pragma unroll
;                     for (int j = 0; j < 4; ++j) { gg[j] = fminf(g[j], 7.0f); ll[j] = __builtin_amdgcn_fmed3f(l[j], -7.0f, 7.0f); }
;                     const f32x4 t = gg * (-1.702f * 1.44269504089f);
; #pragma unroll
;                     for (int j = 0; j < 4; ++j) ex[j] = __builtin_amdgcn_exp2f(t[j]);
;                     const f32x4 d = ex + 1.0f;
; #pragma unroll
;                     for (int j = 0; j < 4; ++j) rc[j] = __builtin_amdgcn_rcpf(d[j]);
;                     a[n] = (gg * rc) * (ll * oscale + oscale); }
;                 int w0 = 0, w1 = 0;
;                 w0 = __builtin_amdgcn_cvt_pk_fp8_f32(a[0][0], a[0][1], w0, false); w0 = __builtin_amdgcn_cvt_pk_fp8_f32(a[0][2], a[0][3], w0, true);
;                 w1 = __builtin_amdgcn_cvt_pk_fp8_f32(a[1][0], a[1][1], w1, false); w1 = __builtin_amdgcn_cvt_pk_fp8_f32(a[1][2], a[1][3], w1, true);
;                 u32x2 w; w.x = (unsigned)w0; w.y = (unsigned)w1; *(u32x2*)rowp = w; }
; template <class Epi, class Sched, bool ALIGN_EPI = false, bool SP2 = false, bool GATHER = false, bool F8 = false>
; __device__ __forceinline__ void gemm_phase(PG8_LAS unsigned char* lds, const Gemm g, const Sched& S, const Epi& E) {
;     ...
;         if (!has_next) break;
;         if (!(Epi::MID && cur.kh == 0)) {
; #pragma unroll
;         for (int a = 0; a < 2; ++a)
; #pragma unroll
;             for (int b = 0; b < 2; ++b)
; #pragma unroll
;                 for (int m = 0; m < 4; ++m)
; #pragma unroll
;                     for (int n = 0; n < 2; ++n) acc[a][b][m][n] = (f32x4){0.f, 0.f, 0.f, 0.f}; }
;         cur = nxt; cA = nA; cB = nB; ++ui;
;         if constexpr (GATHER) { gc0[0] = gn0[0]; gc0[1] = gn0[1]; gc1[0] = gn1[0]; gc1[1] = gn1[1]; }
;         if constexpr (ALIGN_EPI) { if (wr == 1) PG8_BAR; }
	v_exp_f32_e32 v50, v32
	v_mul_f32_e32 v32, 0xc01d265f, v29
	v_add_f32_e32 v31, 1.0, v31
	v_fmamk_f32 v27, v51, 0x3b000000, v3
	v_exp_f32_e32 v51, v32
	v_rcp_f32_e32 v32, v31
	v_add_f32_e32 v31, 1.0, v33
	v_rcp_f32_e32 v33, v31
	v_add_f32_e32 v31, 1.0, v50
	v_med3_f32 v27, v27, s72, v201
	v_rcp_f32_e32 v50, v31
	v_add_f32_e32 v31, 1.0, v51
	v_rcp_f32_e32 v51, v31
	v_pk_mul_f32 v[22:23], v[22:23], v[32:33]
	v_pk_fma_f32 v[26:27], v[26:27], 4.0, 4.0 op_sel_hi:[1,0,0]
	v_fmamk_f32 v31, v53, 0x3b000000, v5
	v_pk_mul_f32 v[22:23], v[26:27], v[22:23]
	v_mov_b32_e32 v26, v163
	v_mov_b32_e32 v27, v163
	v_cvt_pk_fp8_f32 v26, v20, v21
	v_cvt_pk_fp8_f32 v27, v22, v23
	v_med3_f32 v31, v31, s72, v201
	v_pk_mul_f32 v[28:29], v[28:29], v[50:51]
	v_pk_fma_f32 v[20:21], v[30:31], 4.0, 4.0 op_sel_hi:[1,0,0]
	v_cvt_pk_fp8_f32 v26, v24, v25 op_sel:[0,0,1]
	v_pk_mul_f32 v[20:21], v[20:21], v[28:29]
	v_fmamk_f32 v14, v46, 0x3b000000, v14
	v_cvt_pk_fp8_f32 v27, v20, v21 op_sel:[0,0,1]
	v_add_co_u32_e32 v20, vcc, s75, v18
	v_fmamk_f32 v15, v47, 0x3b000000, v15
	s_nop 0
	v_addc_co_u32_e32 v21, vcc, 0, v19, vcc
	v_min_f32_e32 v14, 0x40e00000, v14
	v_min_f32_e32 v15, 0x40e00000, v15
	global_store_dwordx2 v[20:21], v[26:27], off
	v_mul_f32_e32 v20, 0xc01d265f, v14
	v_mul_f32_e32 v21, 0xc01d265f, v15
	v_exp_f32_e32 v20, v20
	v_exp_f32_e32 v21, v21
	v_fmamk_f32 v16, v48, 0x3b000000, v16
	v_fmac_f32_e32 v17, 0x3b000000, v49
	v_min_f32_e32 v16, 0x40e00000, v16
	v_min_f32_e32 v17, 0x40e00000, v17
	v_mul_f32_e32 v22, 0xc01d265f, v16
	v_mul_f32_e32 v23, 0xc01d265f, v17
	v_exp_f32_e32 v22, v22
	v_exp_f32_e32 v23, v23
	v_add_f32_e32 v20, 1.0, v20
	v_add_f32_e32 v21, 1.0, v21
	v_rcp_f32_e32 v20, v20
	v_rcp_f32_e32 v21, v21
	v_fmamk_f32 v10, v42, 0x3b000000, v10
	v_fmamk_f32 v11, v43, 0x3b000000, v11
	v_med3_f32 v10, v10, s72, v201
	v_med3_f32 v11, v11, s72, v201
	v_add_f32_e32 v22, 1.0, v22
	v_add_f32_e32 v23, 1.0, v23
	v_fmamk_f32 v6, v38, 0x3b000000, v6
	v_fmamk_f32 v7, v39, 0x3b000000, v7
	v_rcp_f32_e32 v22, v22
	v_rcp_f32_e32 v23, v23
	v_pk_mul_f32 v[14:15], v[14:15], v[20:21]
	v_pk_fma_f32 v[10:11], v[10:11], 4.0, 4.0 op_sel_hi:[1,0,0]
	v_min_f32_e32 v6, 0x40e00000, v6
	v_min_f32_e32 v7, 0x40e00000, v7
	v_pk_mul_f32 v[10:11], v[10:11], v[14:15]
	v_mul_f32_e32 v14, 0xc01d265f, v6
	v_mul_f32_e32 v15, 0xc01d265f, v7
	v_fmamk_f32 v12, v44, 0x3b000000, v12
	v_fmac_f32_e32 v13, 0x3b000000, v45
	v_exp_f32_e32 v14, v14
	v_exp_f32_e32 v15, v15
	v_med3_f32 v12, v12, s72, v201
	v_med3_f32 v13, v13, s72, v201
	v_fmamk_f32 v8, v40, 0x3b000000, v8
	v_fmac_f32_e32 v9, 0x3b000000, v41
	v_pk_mul_f32 v[16:17], v[16:17], v[22:23]
	v_pk_fma_f32 v[12:13], v[12:13], 4.0, 4.0 op_sel_hi:[1,0,0]
	v_min_f32_e32 v8, 0x40e00000, v8
	v_min_f32_e32 v9, 0x40e00000, v9
	v_pk_mul_f32 v[12:13], v[12:13], v[16:17]
	v_mul_f32_e32 v16, 0xc01d265f, v8
	v_mul_f32_e32 v17, 0xc01d265f, v9
	v_exp_f32_e32 v16, v16
	v_exp_f32_e32 v17, v17
	v_add_f32_e32 v14, 1.0, v14
	v_add_f32_e32 v15, 1.0, v15
	v_rcp_f32_e32 v14, v14
	v_rcp_f32_e32 v15, v15
	v_fmamk_f32 v2, v34, 0x3b000000, v2
	v_fmamk_f32 v3, v35, 0x3b000000, v3
	v_med3_f32 v2, v2, s72, v201
	v_med3_f32 v3, v3, s72, v201
	v_add_f32_e32 v16, 1.0, v16
	v_add_f32_e32 v17, 1.0, v17
	v_rcp_f32_e32 v16, v16
	v_rcp_f32_e32 v17, v17
	v_pk_mul_f32 v[6:7], v[6:7], v[14:15]
	v_pk_fma_f32 v[2:3], v[2:3], 4.0, 4.0 op_sel_hi:[1,0,0]
	v_fmamk_f32 v4, v36, 0x3b000000, v4
	v_pk_mul_f32 v[2:3], v[2:3], v[6:7]
	v_mov_b32_e32 v6, v163
	v_mov_b32_e32 v7, v163
	v_fmac_f32_e32 v5, 0x3b000000, v37
	v_cvt_pk_fp8_f32 v6, v10, v11
	v_cvt_pk_fp8_f32 v7, v2, v3
	v_med3_f32 v4, v4, s72, v201
	v_med3_f32 v5, v5, s72, v201
	v_pk_mul_f32 v[8:9], v[8:9], v[16:17]
	v_pk_fma_f32 v[2:3], v[4:5], 4.0, 4.0 op_sel_hi:[1,0,0]
	v_cvt_pk_fp8_f32 v6, v12, v13 op_sel:[0,0,1]
	v_pk_mul_f32 v[2:3], v[2:3], v[8:9]
	s_nop 0
	v_cvt_pk_fp8_f32 v7, v2, v3 op_sel:[0,0,1]
	v_add_co_u32_e32 v2, vcc, 0x58000, v18
	s_nop 1
	v_addc_co_u32_e32 v3, vcc, 0, v19, vcc
	s_and_b64 vcc, exec, s[0:1]
	s_mov_b64 s[0:1], -1
	global_store_dwordx2 v[2:3], v[6:7], off
	s_cbranch_vccnz .LBB0_1380
	s_andn2_b64 vcc, exec, s[12:13]
	s_cbranch_vccnz .LBB0_1379
	s_barrier
	s_branch .LBB0_1379
